# lean attention loop + spread LDS writes/global loads + running V pointer with immediate offsets and 3-instruction loop test
# speedup vs baseline: 1.0018x; 1.0018x over previous
.Lattn_pa0:
	s_waitcnt lgkmcnt(6)
	v_mfma_f32_16x16x32_bf16 v[64:67], v[160:163], v[96:99], 0
	v_exp_f32_e32 v88, v88
	v_mfma_f32_16x16x32_bf16 v[68:71], v[160:163], v[112:115], 0
	v_exp_f32_e32 v92, v92
	ds_read_b128 v[160:163], v201 offset:20480
	s_add_u32 s15, s22, s12
	s_addc_u32 s14, s23, s13
	s_add_u32 s6, s15, 0x23a50000
	s_addc_u32 s7, s14, 0
	v_mfma_f32_16x16x32_bf16 v[0:3], v[164:167], v[216:219], v[0:3]
	v_cvt_pk_bf16_f32 v242, v80, v81
	v_mfma_f32_16x16x32_bf16 v[4:7], v[164:167], v[238:241], v[4:7]
	v_exp_f32_e32 v89, v89
	ds_read_b128 v[164:167], v209 offset:8192
	s_waitcnt vmcnt(4)
	ds_write_b128 v225, v[152:155] offset:49152
	s_waitcnt lgkmcnt(7)
	v_mfma_f32_16x16x32_bf16 v[68:71], v[168:171], v[116:119], v[68:71]
	v_exp_f32_e32 v93, v93
	v_mfma_f32_16x16x32_bf16 v[64:67], v[168:171], v[100:103], v[64:67]
	v_cvt_pk_bf16_f32 v243, v82, v83
	ds_read_b128 v[168:171], v202 offset:20480
	v_mfma_f32_16x16x32_bf16 v[12:15], v[172:175], v[238:241], v[12:15]
	v_exp_f32_e32 v90, v90
	v_mfma_f32_16x16x32_bf16 v[8:11], v[172:175], v[216:219], v[8:11]
	v_exp_f32_e32 v94, v94
	ds_read_b128 v[172:175], v209 offset:10240
	s_waitcnt lgkmcnt(7)
	v_mfma_f32_16x16x32_bf16 v[64:67], v[176:179], v[104:107], v[64:67]
	v_cvt_pk_bf16_f32 v204, v84, v85
	v_mfma_f32_16x16x32_bf16 v[68:71], v[176:179], v[120:123], v[68:71]
	v_exp_f32_e32 v91, v91
	ds_read_b128 v[176:179], v203 offset:20480
	ds_write_b128 v226, v[156:159] offset:49152
	v_mfma_f32_16x16x32_bf16 v[16:19], v[180:183], v[216:219], v[16:19]
	v_exp_f32_e32 v95, v95
	v_mfma_f32_16x16x32_bf16 v[20:23], v[180:183], v[238:241], v[20:23]
	v_cvt_pk_bf16_f32 v205, v86, v87
	v_add_f32_e32 v220, v220, v88
	ds_read_b128 v[180:183], v209 offset:12288
	s_waitcnt lgkmcnt(8)
	v_mfma_f32_16x16x32_bf16 v[68:71], v[230:233], v[124:127], v[68:71]
	v_add_f32_e32 v221, v221, v92
	v_add_f32_e32 v220, v220, v89
	v_mfma_f32_16x16x32_bf16 v[64:67], v[230:233], v[108:111], v[64:67]
	v_add_f32_e32 v221, v221, v93
	v_cvt_pk_bf16_f32 v244, v88, v89
	ds_read_b128 v[230:233], v246 offset:20480
	v_mfma_f32_16x16x32_bf16 v[28:31], v[234:237], v[238:241], v[28:31]
	v_cvt_pk_bf16_f32 v245, v90, v91
	v_cvt_pk_bf16_f32 v206, v92, v93
	v_mfma_f32_16x16x32_bf16 v[24:27], v[234:237], v[216:219], v[24:27]
	v_cvt_pk_bf16_f32 v207, v94, v95
	ds_read_b128 v[234:237], v209 offset:14336
	ds_write_b64 v227, v[132:133] offset:32768
	s_waitcnt lgkmcnt(9)
	v_mfma_f32_16x16x32_bf16 v[72:75], v[160:163], v[96:99], 0
	v_add_f32_e32 v220, v220, v90
	v_add_f32_e32 v221, v221, v94
	v_mfma_f32_16x16x32_bf16 v[76:79], v[160:163], v[112:115], 0
	v_add_f32_e32 v220, v220, v91
	v_add_f32_e32 v221, v221, v95
	ds_read_b128 v[160:163], v201 offset:24576
	v_mfma_f32_16x16x32_bf16 v[32:35], v[164:167], v[216:219], v[32:35]
	v_add_f32_e32 v194, v194, v220
	v_add_f32_e32 v195, v195, v221
	v_mfma_f32_16x16x32_bf16 v[36:39], v[164:167], v[238:241], v[36:39]
	v_exp_f32_e32 v64, v64
	ds_read_b128 v[164:167], v210 offset:0
	s_waitcnt lgkmcnt(8)
	v_mfma_f32_16x16x32_bf16 v[76:79], v[168:171], v[116:119], v[76:79]
	v_exp_f32_e32 v68, v68
	v_mfma_f32_16x16x32_bf16 v[72:75], v[168:171], v[100:103], v[72:75]
	v_exp_f32_e32 v65, v65
	ds_read_b128 v[168:171], v202 offset:24576
	ds_write_b64 v228, v[134:135] offset:32768
	v_mfma_f32_16x16x32_bf16 v[44:47], v[172:175], v[238:241], v[44:47]
	v_exp_f32_e32 v69, v69
	v_mfma_f32_16x16x32_bf16 v[40:43], v[172:175], v[216:219], v[40:43]
	v_exp_f32_e32 v66, v66
	ds_read_b128 v[172:175], v210 offset:2048
	s_waitcnt lgkmcnt(8)
	v_mfma_f32_16x16x32_bf16 v[72:75], v[176:179], v[104:107], v[72:75]
	v_exp_f32_e32 v70, v70
	v_mfma_f32_16x16x32_bf16 v[76:79], v[176:179], v[120:123], v[76:79]
	v_exp_f32_e32 v67, v67
	ds_read_b128 v[176:179], v203 offset:24576
	v_mfma_f32_16x16x32_bf16 v[48:51], v[180:183], v[216:219], v[48:51]
	v_exp_f32_e32 v71, v71
	v_mfma_f32_16x16x32_bf16 v[52:55], v[180:183], v[238:241], v[52:55]
	v_add_f32_e32 v220, v64, v65
	ds_read_b128 v[180:183], v210 offset:4096
	ds_write_b64 v229, v[128:129] offset:32768
	s_waitcnt lgkmcnt(9)
	v_mfma_f32_16x16x32_bf16 v[76:79], v[230:233], v[124:127], v[76:79]
	v_add_f32_e32 v221, v68, v69
	v_mfma_f32_16x16x32_bf16 v[72:75], v[230:233], v[108:111], v[72:75]
	v_add_f32_e32 v220, v220, v66
	ds_read_b128 v[230:233], v246 offset:24576
	v_mfma_f32_16x16x32_bf16 v[60:63], v[234:237], v[238:241], v[60:63]
	v_add_f32_e32 v221, v221, v70
	v_add_f32_e32 v220, v220, v67
	v_mfma_f32_16x16x32_bf16 v[56:59], v[234:237], v[216:219], v[56:59]
	v_add_f32_e32 v221, v221, v71
	ds_read_b128 v[234:237], v210 offset:6144
	s_waitcnt lgkmcnt(8)
	v_mfma_f32_16x16x32_bf16 v[80:83], v[160:163], v[96:99], 0
	v_exp_f32_e32 v72, v72
	v_mfma_f32_16x16x32_bf16 v[84:87], v[160:163], v[112:115], 0
	v_exp_f32_e32 v76, v76
	ds_read_b128 v[160:163], v201 offset:28672
	ds_write_b64 v184, v[130:131] offset:32768
	v_mfma_f32_16x16x32_bf16 v[0:3], v[164:167], v[242:245], v[0:3]
	v_exp_f32_e32 v73, v73
	v_mfma_f32_16x16x32_bf16 v[4:7], v[164:167], v[204:207], v[4:7]
	v_exp_f32_e32 v77, v77
	ds_read_b128 v[164:167], v210 offset:8192
	s_waitcnt lgkmcnt(8)
	v_mfma_f32_16x16x32_bf16 v[84:87], v[168:171], v[116:119], v[84:87]
	v_exp_f32_e32 v74, v74
	v_mfma_f32_16x16x32_bf16 v[80:83], v[168:171], v[100:103], v[80:83]
	v_exp_f32_e32 v78, v78
	ds_read_b128 v[168:171], v202 offset:28672
	v_mfma_f32_16x16x32_bf16 v[12:15], v[172:175], v[204:207], v[12:15]
	v_exp_f32_e32 v75, v75
	v_mfma_f32_16x16x32_bf16 v[8:11], v[172:175], v[242:245], v[8:11]
	v_exp_f32_e32 v79, v79
	ds_read_b128 v[172:175], v210 offset:10240
	global_load_dwordx4 v[132:135], v198, s[8:9]
	s_waitcnt lgkmcnt(8)
	v_mfma_f32_16x16x32_bf16 v[80:83], v[176:179], v[104:107], v[80:83]
	v_add_f32_e32 v220, v220, v72
	v_add_f32_e32 v221, v221, v76
	v_mfma_f32_16x16x32_bf16 v[84:87], v[176:179], v[120:123], v[84:87]
	v_add_f32_e32 v220, v220, v73
	ds_read_b128 v[176:179], v203 offset:28672
	v_mfma_f32_16x16x32_bf16 v[16:19], v[180:183], v[242:245], v[16:19]
	v_add_f32_e32 v221, v221, v77
	v_add_f32_e32 v220, v220, v74
	v_mfma_f32_16x16x32_bf16 v[20:23], v[180:183], v[204:207], v[20:23]
	v_add_f32_e32 v221, v221, v78
	ds_read_b128 v[180:183], v210 offset:12288
	s_waitcnt lgkmcnt(7)
	v_mfma_f32_16x16x32_bf16 v[84:87], v[230:233], v[124:127], v[84:87]
	v_add_f32_e32 v220, v220, v75
	v_add_f32_e32 v221, v221, v79
	v_mfma_f32_16x16x32_bf16 v[80:83], v[230:233], v[108:111], v[80:83]
	v_cvt_pk_bf16_f32 v216, v64, v65
	ds_read_b128 v[230:233], v246 offset:28672
	global_load_dwordx4 v[128:131], v199, s[8:9]
	v_mfma_f32_16x16x32_bf16 v[28:31], v[234:237], v[204:207], v[28:31]
	v_cvt_pk_bf16_f32 v217, v66, v67
	v_cvt_pk_bf16_f32 v238, v68, v69
	v_mfma_f32_16x16x32_bf16 v[24:27], v[234:237], v[242:245], v[24:27]
	v_cvt_pk_bf16_f32 v239, v70, v71
	ds_read_b128 v[234:237], v210 offset:14336
	s_waitcnt lgkmcnt(6)
	v_mfma_f32_16x16x32_bf16 v[88:91], v[160:163], v[96:99], 0
	v_exp_f32_e32 v80, v80
	v_mfma_f32_16x16x32_bf16 v[92:95], v[160:163], v[112:115], 0
	v_exp_f32_e32 v84, v84
	ds_read_b128 v[160:163], v201 offset:32768
	v_mfma_f32_16x16x32_bf16 v[32:35], v[164:167], v[242:245], v[32:35]
	v_exp_f32_e32 v81, v81
	v_mfma_f32_16x16x32_bf16 v[36:39], v[164:167], v[204:207], v[36:39]
	v_exp_f32_e32 v85, v85
	ds_read_b128 v[164:167], v209 offset:16384
	global_load_dwordx4 v[152:155], v196, s[6:7]
	s_waitcnt lgkmcnt(6)
	v_mfma_f32_16x16x32_bf16 v[92:95], v[168:171], v[116:119], v[92:95]
	v_exp_f32_e32 v82, v82
	v_mfma_f32_16x16x32_bf16 v[88:91], v[168:171], v[100:103], v[88:91]
	v_exp_f32_e32 v86, v86
	ds_read_b128 v[168:171], v202 offset:32768
	v_mfma_f32_16x16x32_bf16 v[44:47], v[172:175], v[204:207], v[44:47]
	v_exp_f32_e32 v83, v83
	v_mfma_f32_16x16x32_bf16 v[40:43], v[172:175], v[242:245], v[40:43]
	v_exp_f32_e32 v87, v87
	ds_read_b128 v[172:175], v209 offset:18432
	s_waitcnt lgkmcnt(6)
	v_mfma_f32_16x16x32_bf16 v[88:91], v[176:179], v[104:107], v[88:91]
	v_add_f32_e32 v220, v220, v80
	v_add_f32_e32 v221, v221, v84
	v_mfma_f32_16x16x32_bf16 v[92:95], v[176:179], v[120:123], v[92:95]
	v_add_f32_e32 v220, v220, v81
	ds_read_b128 v[176:179], v203 offset:32768
	global_load_dwordx4 v[156:159], v197, s[6:7]
	v_mfma_f32_16x16x32_bf16 v[48:51], v[180:183], v[242:245], v[48:51]
	v_add_f32_e32 v221, v221, v85
	v_add_f32_e32 v220, v220, v82
	v_mfma_f32_16x16x32_bf16 v[52:55], v[180:183], v[204:207], v[52:55]
	v_add_f32_e32 v221, v221, v86
	ds_read_b128 v[180:183], v209 offset:20480
	s_waitcnt lgkmcnt(6)
	v_mfma_f32_16x16x32_bf16 v[92:95], v[230:233], v[124:127], v[92:95]
	v_add_f32_e32 v220, v220, v83
	v_add_f32_e32 v221, v221, v87
	v_mfma_f32_16x16x32_bf16 v[88:91], v[230:233], v[108:111], v[88:91]
	v_cvt_pk_bf16_f32 v218, v72, v73
	ds_read_b128 v[230:233], v246 offset:32768
	v_mfma_f32_16x16x32_bf16 v[60:63], v[234:237], v[204:207], v[60:63]
	v_cvt_pk_bf16_f32 v219, v74, v75
	v_cvt_pk_bf16_f32 v240, v76, v77
	v_mfma_f32_16x16x32_bf16 v[56:59], v[234:237], v[242:245], v[56:59]
	v_cvt_pk_bf16_f32 v241, v78, v79
	ds_read_b128 v[234:237], v209 offset:22528
	s_setprio 0
	s_waitcnt lgkmcnt(6)
	v_mfma_f32_16x16x32_bf16 v[64:67], v[160:163], v[96:99], 0
	v_exp_f32_e32 v88, v88
	v_mfma_f32_16x16x32_bf16 v[68:71], v[160:163], v[112:115], 0
	v_exp_f32_e32 v92, v92
	ds_read_b128 v[160:163], v201 offset:36864
	s_add_u32 s6, s15, 0x23a60000
	s_addc_u32 s7, s14, 0
	v_mfma_f32_16x16x32_bf16 v[0:3], v[164:167], v[216:219], v[0:3]
	v_cvt_pk_bf16_f32 v242, v80, v81
	v_mfma_f32_16x16x32_bf16 v[4:7], v[164:167], v[238:241], v[4:7]
	v_exp_f32_e32 v89, v89
	ds_read_b128 v[164:167], v209 offset:24576
	s_waitcnt vmcnt(4)
	ds_write_b128 v225, v[136:139] offset:0
	s_waitcnt lgkmcnt(7)
	v_mfma_f32_16x16x32_bf16 v[68:71], v[168:171], v[116:119], v[68:71]
	v_exp_f32_e32 v93, v93
	v_mfma_f32_16x16x32_bf16 v[64:67], v[168:171], v[100:103], v[64:67]
	v_cvt_pk_bf16_f32 v243, v82, v83
	ds_read_b128 v[168:171], v202 offset:36864
	v_mfma_f32_16x16x32_bf16 v[12:15], v[172:175], v[238:241], v[12:15]
	v_exp_f32_e32 v90, v90
	v_mfma_f32_16x16x32_bf16 v[8:11], v[172:175], v[216:219], v[8:11]
	v_exp_f32_e32 v94, v94
	ds_read_b128 v[172:175], v209 offset:26624
	s_waitcnt lgkmcnt(7)
	v_mfma_f32_16x16x32_bf16 v[64:67], v[176:179], v[104:107], v[64:67]
	v_cvt_pk_bf16_f32 v204, v84, v85
	v_mfma_f32_16x16x32_bf16 v[68:71], v[176:179], v[120:123], v[68:71]
	v_exp_f32_e32 v91, v91
	ds_read_b128 v[176:179], v203 offset:36864
	ds_write_b128 v226, v[140:143] offset:0
	v_mfma_f32_16x16x32_bf16 v[16:19], v[180:183], v[216:219], v[16:19]
	v_exp_f32_e32 v95, v95
	v_mfma_f32_16x16x32_bf16 v[20:23], v[180:183], v[238:241], v[20:23]
	v_cvt_pk_bf16_f32 v205, v86, v87
	v_add_f32_e32 v220, v220, v88
	ds_read_b128 v[180:183], v209 offset:28672
	s_waitcnt lgkmcnt(8)
	v_mfma_f32_16x16x32_bf16 v[68:71], v[230:233], v[124:127], v[68:71]
	v_add_f32_e32 v221, v221, v92
	v_add_f32_e32 v220, v220, v89
	v_mfma_f32_16x16x32_bf16 v[64:67], v[230:233], v[108:111], v[64:67]
	v_add_f32_e32 v221, v221, v93
	v_cvt_pk_bf16_f32 v244, v88, v89
	ds_read_b128 v[230:233], v246 offset:36864
	v_mfma_f32_16x16x32_bf16 v[28:31], v[234:237], v[238:241], v[28:31]
	v_cvt_pk_bf16_f32 v245, v90, v91
	v_cvt_pk_bf16_f32 v206, v92, v93
	v_mfma_f32_16x16x32_bf16 v[24:27], v[234:237], v[216:219], v[24:27]
	v_cvt_pk_bf16_f32 v207, v94, v95
	ds_read_b128 v[234:237], v209 offset:30720
	ds_write_b64 v227, v[148:149] offset:49152
	s_waitcnt lgkmcnt(9)
	v_mfma_f32_16x16x32_bf16 v[72:75], v[160:163], v[96:99], 0
	v_add_f32_e32 v220, v220, v90
	v_add_f32_e32 v221, v221, v94
	v_mfma_f32_16x16x32_bf16 v[76:79], v[160:163], v[112:115], 0
	v_add_f32_e32 v220, v220, v91
	v_add_f32_e32 v221, v221, v95
	ds_read_b128 v[160:163], v201 offset:40960
	v_mfma_f32_16x16x32_bf16 v[32:35], v[164:167], v[216:219], v[32:35]
	v_add_f32_e32 v194, v194, v220
	v_add_f32_e32 v195, v195, v221
	v_mfma_f32_16x16x32_bf16 v[36:39], v[164:167], v[238:241], v[36:39]
	v_exp_f32_e32 v64, v64
	ds_read_b128 v[164:167], v210 offset:16384
	s_waitcnt lgkmcnt(8)
	v_mfma_f32_16x16x32_bf16 v[76:79], v[168:171], v[116:119], v[76:79]
	v_exp_f32_e32 v68, v68
	v_mfma_f32_16x16x32_bf16 v[72:75], v[168:171], v[100:103], v[72:75]
	v_exp_f32_e32 v65, v65
	ds_read_b128 v[168:171], v202 offset:40960
	ds_write_b64 v228, v[150:151] offset:49152
	v_mfma_f32_16x16x32_bf16 v[44:47], v[172:175], v[238:241], v[44:47]
	v_exp_f32_e32 v69, v69
	v_mfma_f32_16x16x32_bf16 v[40:43], v[172:175], v[216:219], v[40:43]
	v_exp_f32_e32 v66, v66
	ds_read_b128 v[172:175], v210 offset:18432
	s_waitcnt lgkmcnt(8)
	v_mfma_f32_16x16x32_bf16 v[72:75], v[176:179], v[104:107], v[72:75]
	v_exp_f32_e32 v70, v70
	v_mfma_f32_16x16x32_bf16 v[76:79], v[176:179], v[120:123], v[76:79]
	v_exp_f32_e32 v67, v67
	ds_read_b128 v[176:179], v203 offset:40960
	v_mfma_f32_16x16x32_bf16 v[48:51], v[180:183], v[216:219], v[48:51]
	v_exp_f32_e32 v71, v71
	v_mfma_f32_16x16x32_bf16 v[52:55], v[180:183], v[238:241], v[52:55]
	v_add_f32_e32 v220, v64, v65
	ds_read_b128 v[180:183], v210 offset:20480
	ds_write_b64 v229, v[144:145] offset:49152
	s_waitcnt lgkmcnt(9)
	v_mfma_f32_16x16x32_bf16 v[76:79], v[230:233], v[124:127], v[76:79]
	v_add_f32_e32 v221, v68, v69
	v_mfma_f32_16x16x32_bf16 v[72:75], v[230:233], v[108:111], v[72:75]
	v_add_f32_e32 v220, v220, v66
	ds_read_b128 v[230:233], v246 offset:40960
	v_mfma_f32_16x16x32_bf16 v[60:63], v[234:237], v[238:241], v[60:63]
	v_add_f32_e32 v221, v221, v70
	v_add_f32_e32 v220, v220, v67
	v_mfma_f32_16x16x32_bf16 v[56:59], v[234:237], v[216:219], v[56:59]
	v_add_f32_e32 v221, v221, v71
	ds_read_b128 v[234:237], v210 offset:22528
	s_waitcnt lgkmcnt(8)
	v_mfma_f32_16x16x32_bf16 v[80:83], v[160:163], v[96:99], 0
	v_exp_f32_e32 v72, v72
	v_mfma_f32_16x16x32_bf16 v[84:87], v[160:163], v[112:115], 0
	v_exp_f32_e32 v76, v76
	ds_read_b128 v[160:163], v201 offset:45056
	ds_write_b64 v184, v[146:147] offset:49152
	v_mfma_f32_16x16x32_bf16 v[0:3], v[164:167], v[242:245], v[0:3]
	v_exp_f32_e32 v73, v73
	v_mfma_f32_16x16x32_bf16 v[4:7], v[164:167], v[204:207], v[4:7]
	v_exp_f32_e32 v77, v77
	ds_read_b128 v[164:167], v210 offset:24576
	s_waitcnt lgkmcnt(8)
	v_mfma_f32_16x16x32_bf16 v[84:87], v[168:171], v[116:119], v[84:87]
	v_exp_f32_e32 v74, v74
	v_mfma_f32_16x16x32_bf16 v[80:83], v[168:171], v[100:103], v[80:83]
	v_exp_f32_e32 v78, v78
	ds_read_b128 v[168:171], v202 offset:45056
	v_mfma_f32_16x16x32_bf16 v[12:15], v[172:175], v[204:207], v[12:15]
	v_exp_f32_e32 v75, v75
	v_mfma_f32_16x16x32_bf16 v[8:11], v[172:175], v[242:245], v[8:11]
	v_exp_f32_e32 v79, v79
	ds_read_b128 v[172:175], v210 offset:26624
	global_load_dwordx4 v[148:151], v198, s[8:9] offset:128
	s_waitcnt lgkmcnt(8)
	v_mfma_f32_16x16x32_bf16 v[80:83], v[176:179], v[104:107], v[80:83]
	v_add_f32_e32 v220, v220, v72
	v_add_f32_e32 v221, v221, v76
	v_mfma_f32_16x16x32_bf16 v[84:87], v[176:179], v[120:123], v[84:87]
	v_add_f32_e32 v220, v220, v73
	ds_read_b128 v[176:179], v203 offset:45056
	v_mfma_f32_16x16x32_bf16 v[16:19], v[180:183], v[242:245], v[16:19]
	v_add_f32_e32 v221, v221, v77
	v_add_f32_e32 v220, v220, v74
	v_mfma_f32_16x16x32_bf16 v[20:23], v[180:183], v[204:207], v[20:23]
	v_add_f32_e32 v221, v221, v78
	ds_read_b128 v[180:183], v210 offset:28672
	s_waitcnt lgkmcnt(7)
	v_mfma_f32_16x16x32_bf16 v[84:87], v[230:233], v[124:127], v[84:87]
	v_add_f32_e32 v220, v220, v75
	v_add_f32_e32 v221, v221, v79
	v_mfma_f32_16x16x32_bf16 v[80:83], v[230:233], v[108:111], v[80:83]
	v_cvt_pk_bf16_f32 v216, v64, v65
	ds_read_b128 v[230:233], v246 offset:45056
	global_load_dwordx4 v[144:147], v199, s[8:9] offset:128
	v_mfma_f32_16x16x32_bf16 v[28:31], v[234:237], v[204:207], v[28:31]
	v_cvt_pk_bf16_f32 v217, v66, v67
	v_cvt_pk_bf16_f32 v238, v68, v69
	v_mfma_f32_16x16x32_bf16 v[24:27], v[234:237], v[242:245], v[24:27]
	v_cvt_pk_bf16_f32 v239, v70, v71
	ds_read_b128 v[234:237], v210 offset:30720
	s_waitcnt lgkmcnt(6)
	v_mfma_f32_16x16x32_bf16 v[88:91], v[160:163], v[96:99], 0
	v_exp_f32_e32 v80, v80
	v_mfma_f32_16x16x32_bf16 v[92:95], v[160:163], v[112:115], 0
	v_exp_f32_e32 v84, v84
	v_mfma_f32_16x16x32_bf16 v[32:35], v[164:167], v[242:245], v[32:35]
	v_exp_f32_e32 v81, v81
	v_mfma_f32_16x16x32_bf16 v[36:39], v[164:167], v[204:207], v[36:39]
	v_exp_f32_e32 v85, v85
	global_load_dwordx4 v[136:139], v196, s[6:7]
	s_waitcnt lgkmcnt(4)
	v_mfma_f32_16x16x32_bf16 v[92:95], v[168:171], v[116:119], v[92:95]
	v_exp_f32_e32 v82, v82
	v_mfma_f32_16x16x32_bf16 v[88:91], v[168:171], v[100:103], v[88:91]
	v_exp_f32_e32 v86, v86
	v_mfma_f32_16x16x32_bf16 v[44:47], v[172:175], v[204:207], v[44:47]
	v_exp_f32_e32 v83, v83
	v_mfma_f32_16x16x32_bf16 v[40:43], v[172:175], v[242:245], v[40:43]
	v_exp_f32_e32 v87, v87
	s_waitcnt lgkmcnt(3)
	v_mfma_f32_16x16x32_bf16 v[88:91], v[176:179], v[104:107], v[88:91]
	v_add_f32_e32 v220, v220, v80
	v_add_f32_e32 v221, v221, v84
	v_mfma_f32_16x16x32_bf16 v[92:95], v[176:179], v[120:123], v[92:95]
	v_add_f32_e32 v220, v220, v81
	global_load_dwordx4 v[140:143], v197, s[6:7]
	s_waitcnt lgkmcnt(0)
	s_barrier
	ds_read_b128 v[160:163], v201 offset:49152
	ds_read_b128 v[164:167], v209 offset:32768
	ds_read_b128 v[168:171], v202 offset:49152
	ds_read_b128 v[172:175], v209 offset:34816
	ds_read_b128 v[176:179], v203 offset:49152
	v_mfma_f32_16x16x32_bf16 v[48:51], v[180:183], v[242:245], v[48:51]
	v_add_f32_e32 v221, v221, v85
	v_add_f32_e32 v220, v220, v82
	v_mfma_f32_16x16x32_bf16 v[52:55], v[180:183], v[204:207], v[52:55]
	v_add_f32_e32 v221, v221, v86
	ds_read_b128 v[180:183], v209 offset:36864
	v_mfma_f32_16x16x32_bf16 v[92:95], v[230:233], v[124:127], v[92:95]
	v_add_f32_e32 v220, v220, v83
	v_add_f32_e32 v221, v221, v87
	v_mfma_f32_16x16x32_bf16 v[88:91], v[230:233], v[108:111], v[88:91]
	v_cvt_pk_bf16_f32 v218, v72, v73
	ds_read_b128 v[230:233], v246 offset:49152
	v_mfma_f32_16x16x32_bf16 v[60:63], v[234:237], v[204:207], v[60:63]
	v_cvt_pk_bf16_f32 v219, v74, v75
	v_cvt_pk_bf16_f32 v240, v76, v77
	v_mfma_f32_16x16x32_bf16 v[56:59], v[234:237], v[242:245], v[56:59]
	v_cvt_pk_bf16_f32 v241, v78, v79
	ds_read_b128 v[234:237], v209 offset:38912
	s_cmp_eq_u32 s100, 0
	s_cbranch_scc1 .Lattn_pa2
	s_setprio 1
.Lattn_pa2:
	s_waitcnt lgkmcnt(6)
	v_mfma_f32_16x16x32_bf16 v[64:67], v[160:163], v[96:99], 0
	v_exp_f32_e32 v88, v88
	v_mfma_f32_16x16x32_bf16 v[68:71], v[160:163], v[112:115], 0
	v_exp_f32_e32 v92, v92
	ds_read_b128 v[160:163], v201 offset:53248
	s_add_u32 s6, s15, 0x23a70000
	s_addc_u32 s7, s14, 0
	v_mfma_f32_16x16x32_bf16 v[0:3], v[164:167], v[216:219], v[0:3]
	v_cvt_pk_bf16_f32 v242, v80, v81
	v_mfma_f32_16x16x32_bf16 v[4:7], v[164:167], v[238:241], v[4:7]
	v_exp_f32_e32 v89, v89
	ds_read_b128 v[164:167], v209 offset:40960
	s_waitcnt vmcnt(4)
	ds_write_b128 v225, v[152:155] offset:16384
	s_waitcnt lgkmcnt(7)
	v_mfma_f32_16x16x32_bf16 v[68:71], v[168:171], v[116:119], v[68:71]
	v_exp_f32_e32 v93, v93
	v_mfma_f32_16x16x32_bf16 v[64:67], v[168:171], v[100:103], v[64:67]
	v_cvt_pk_bf16_f32 v243, v82, v83
	ds_read_b128 v[168:171], v202 offset:53248
	v_mfma_f32_16x16x32_bf16 v[12:15], v[172:175], v[238:241], v[12:15]
	v_exp_f32_e32 v90, v90
	v_mfma_f32_16x16x32_bf16 v[8:11], v[172:175], v[216:219], v[8:11]
	v_exp_f32_e32 v94, v94
	ds_read_b128 v[172:175], v209 offset:43008
	s_waitcnt lgkmcnt(7)
	v_mfma_f32_16x16x32_bf16 v[64:67], v[176:179], v[104:107], v[64:67]
	v_cvt_pk_bf16_f32 v204, v84, v85
	v_mfma_f32_16x16x32_bf16 v[68:71], v[176:179], v[120:123], v[68:71]
	v_exp_f32_e32 v91, v91
	ds_read_b128 v[176:179], v203 offset:53248
	ds_write_b128 v226, v[156:159] offset:16384
	v_mfma_f32_16x16x32_bf16 v[16:19], v[180:183], v[216:219], v[16:19]
	v_exp_f32_e32 v95, v95
	v_mfma_f32_16x16x32_bf16 v[20:23], v[180:183], v[238:241], v[20:23]
	v_cvt_pk_bf16_f32 v205, v86, v87
	v_add_f32_e32 v220, v220, v88
	ds_read_b128 v[180:183], v209 offset:45056
	s_waitcnt lgkmcnt(8)
	v_mfma_f32_16x16x32_bf16 v[68:71], v[230:233], v[124:127], v[68:71]
	v_add_f32_e32 v221, v221, v92
	v_add_f32_e32 v220, v220, v89
	v_mfma_f32_16x16x32_bf16 v[64:67], v[230:233], v[108:111], v[64:67]
	v_add_f32_e32 v221, v221, v93
	v_cvt_pk_bf16_f32 v244, v88, v89
	ds_read_b128 v[230:233], v246 offset:53248
	v_mfma_f32_16x16x32_bf16 v[28:31], v[234:237], v[238:241], v[28:31]
	v_cvt_pk_bf16_f32 v245, v90, v91
	v_cvt_pk_bf16_f32 v206, v92, v93
	v_mfma_f32_16x16x32_bf16 v[24:27], v[234:237], v[216:219], v[24:27]
	v_cvt_pk_bf16_f32 v207, v94, v95
	ds_read_b128 v[234:237], v209 offset:47104
	ds_write_b64 v227, v[132:133] offset:0
	s_waitcnt lgkmcnt(9)
	v_mfma_f32_16x16x32_bf16 v[72:75], v[160:163], v[96:99], 0
	v_add_f32_e32 v220, v220, v90
	v_add_f32_e32 v221, v221, v94
	v_mfma_f32_16x16x32_bf16 v[76:79], v[160:163], v[112:115], 0
	v_add_f32_e32 v220, v220, v91
	v_add_f32_e32 v221, v221, v95
	ds_read_b128 v[160:163], v201 offset:57344
	v_mfma_f32_16x16x32_bf16 v[32:35], v[164:167], v[216:219], v[32:35]
	v_add_f32_e32 v194, v194, v220
	v_add_f32_e32 v195, v195, v221
	v_mfma_f32_16x16x32_bf16 v[36:39], v[164:167], v[238:241], v[36:39]
	v_exp_f32_e32 v64, v64
	ds_read_b128 v[164:167], v210 offset:32768
	s_waitcnt lgkmcnt(8)
	v_mfma_f32_16x16x32_bf16 v[76:79], v[168:171], v[116:119], v[76:79]
	v_exp_f32_e32 v68, v68
	v_mfma_f32_16x16x32_bf16 v[72:75], v[168:171], v[100:103], v[72:75]
	v_exp_f32_e32 v65, v65
	ds_read_b128 v[168:171], v202 offset:57344
	ds_write_b64 v228, v[134:135] offset:0
	v_mfma_f32_16x16x32_bf16 v[44:47], v[172:175], v[238:241], v[44:47]
	v_exp_f32_e32 v69, v69
	v_mfma_f32_16x16x32_bf16 v[40:43], v[172:175], v[216:219], v[40:43]
	v_exp_f32_e32 v66, v66
	ds_read_b128 v[172:175], v210 offset:34816
	s_waitcnt lgkmcnt(8)
	v_mfma_f32_16x16x32_bf16 v[72:75], v[176:179], v[104:107], v[72:75]
	v_exp_f32_e32 v70, v70
	v_mfma_f32_16x16x32_bf16 v[76:79], v[176:179], v[120:123], v[76:79]
	v_exp_f32_e32 v67, v67
	ds_read_b128 v[176:179], v203 offset:57344
	v_mfma_f32_16x16x32_bf16 v[48:51], v[180:183], v[216:219], v[48:51]
	v_exp_f32_e32 v71, v71
	v_mfma_f32_16x16x32_bf16 v[52:55], v[180:183], v[238:241], v[52:55]
	v_add_f32_e32 v220, v64, v65
	ds_read_b128 v[180:183], v210 offset:36864
	ds_write_b64 v229, v[128:129] offset:0
	s_waitcnt lgkmcnt(9)
	v_mfma_f32_16x16x32_bf16 v[76:79], v[230:233], v[124:127], v[76:79]
	v_add_f32_e32 v221, v68, v69
	v_mfma_f32_16x16x32_bf16 v[72:75], v[230:233], v[108:111], v[72:75]
	v_add_f32_e32 v220, v220, v66
	ds_read_b128 v[230:233], v246 offset:57344
	v_mfma_f32_16x16x32_bf16 v[60:63], v[234:237], v[238:241], v[60:63]
	v_add_f32_e32 v221, v221, v70
	v_add_f32_e32 v220, v220, v67
	v_mfma_f32_16x16x32_bf16 v[56:59], v[234:237], v[216:219], v[56:59]
	v_add_f32_e32 v221, v221, v71
	ds_read_b128 v[234:237], v210 offset:38912
	s_waitcnt lgkmcnt(8)
	v_mfma_f32_16x16x32_bf16 v[80:83], v[160:163], v[96:99], 0
	v_exp_f32_e32 v72, v72
	v_mfma_f32_16x16x32_bf16 v[84:87], v[160:163], v[112:115], 0
	v_exp_f32_e32 v76, v76
	ds_read_b128 v[160:163], v201 offset:61440
	ds_write_b64 v184, v[130:131] offset:0
	v_mfma_f32_16x16x32_bf16 v[0:3], v[164:167], v[242:245], v[0:3]
	v_exp_f32_e32 v73, v73
	v_mfma_f32_16x16x32_bf16 v[4:7], v[164:167], v[204:207], v[4:7]
	v_exp_f32_e32 v77, v77
	ds_read_b128 v[164:167], v210 offset:40960
	s_waitcnt lgkmcnt(8)
	v_mfma_f32_16x16x32_bf16 v[84:87], v[168:171], v[116:119], v[84:87]
	v_exp_f32_e32 v74, v74
	v_mfma_f32_16x16x32_bf16 v[80:83], v[168:171], v[100:103], v[80:83]
	v_exp_f32_e32 v78, v78
	ds_read_b128 v[168:171], v202 offset:61440
	v_mfma_f32_16x16x32_bf16 v[12:15], v[172:175], v[204:207], v[12:15]
	v_exp_f32_e32 v75, v75
	v_mfma_f32_16x16x32_bf16 v[8:11], v[172:175], v[242:245], v[8:11]
	v_exp_f32_e32 v79, v79
	ds_read_b128 v[172:175], v210 offset:43008
	global_load_dwordx4 v[132:135], v198, s[8:9] offset:256
	s_waitcnt lgkmcnt(8)
	v_mfma_f32_16x16x32_bf16 v[80:83], v[176:179], v[104:107], v[80:83]
	v_add_f32_e32 v220, v220, v72
	v_add_f32_e32 v221, v221, v76
	v_mfma_f32_16x16x32_bf16 v[84:87], v[176:179], v[120:123], v[84:87]
	v_add_f32_e32 v220, v220, v73
	ds_read_b128 v[176:179], v203 offset:61440
	v_mfma_f32_16x16x32_bf16 v[16:19], v[180:183], v[242:245], v[16:19]
	v_add_f32_e32 v221, v221, v77
	v_add_f32_e32 v220, v220, v74
	v_mfma_f32_16x16x32_bf16 v[20:23], v[180:183], v[204:207], v[20:23]
	v_add_f32_e32 v221, v221, v78
	ds_read_b128 v[180:183], v210 offset:45056
	s_waitcnt lgkmcnt(7)
	v_mfma_f32_16x16x32_bf16 v[84:87], v[230:233], v[124:127], v[84:87]
	v_add_f32_e32 v220, v220, v75
	v_add_f32_e32 v221, v221, v79
	v_mfma_f32_16x16x32_bf16 v[80:83], v[230:233], v[108:111], v[80:83]
	v_cvt_pk_bf16_f32 v216, v64, v65
	ds_read_b128 v[230:233], v246 offset:61440
	global_load_dwordx4 v[128:131], v199, s[8:9] offset:256
	v_mfma_f32_16x16x32_bf16 v[28:31], v[234:237], v[204:207], v[28:31]
	v_cvt_pk_bf16_f32 v217, v66, v67
	v_cvt_pk_bf16_f32 v238, v68, v69
	v_mfma_f32_16x16x32_bf16 v[24:27], v[234:237], v[242:245], v[24:27]
	v_cvt_pk_bf16_f32 v239, v70, v71
	ds_read_b128 v[234:237], v210 offset:47104
	s_waitcnt lgkmcnt(6)
	v_mfma_f32_16x16x32_bf16 v[88:91], v[160:163], v[96:99], 0
	v_exp_f32_e32 v80, v80
	v_mfma_f32_16x16x32_bf16 v[92:95], v[160:163], v[112:115], 0
	v_exp_f32_e32 v84, v84
	ds_read_b128 v[160:163], v201 offset:0
	v_mfma_f32_16x16x32_bf16 v[32:35], v[164:167], v[242:245], v[32:35]
	v_exp_f32_e32 v81, v81
	v_mfma_f32_16x16x32_bf16 v[36:39], v[164:167], v[204:207], v[36:39]
	v_exp_f32_e32 v85, v85
	ds_read_b128 v[164:167], v209 offset:49152
	global_load_dwordx4 v[152:155], v196, s[6:7]
	s_waitcnt lgkmcnt(6)
	v_mfma_f32_16x16x32_bf16 v[92:95], v[168:171], v[116:119], v[92:95]
	v_exp_f32_e32 v82, v82
	v_mfma_f32_16x16x32_bf16 v[88:91], v[168:171], v[100:103], v[88:91]
	v_exp_f32_e32 v86, v86
	ds_read_b128 v[168:171], v202 offset:0
	v_mfma_f32_16x16x32_bf16 v[44:47], v[172:175], v[204:207], v[44:47]
	v_exp_f32_e32 v83, v83
	v_mfma_f32_16x16x32_bf16 v[40:43], v[172:175], v[242:245], v[40:43]
	v_exp_f32_e32 v87, v87
	ds_read_b128 v[172:175], v209 offset:51200
	s_waitcnt lgkmcnt(6)
	v_mfma_f32_16x16x32_bf16 v[88:91], v[176:179], v[104:107], v[88:91]
	v_add_f32_e32 v220, v220, v80
	v_add_f32_e32 v221, v221, v84
	v_mfma_f32_16x16x32_bf16 v[92:95], v[176:179], v[120:123], v[92:95]
	v_add_f32_e32 v220, v220, v81
	ds_read_b128 v[176:179], v203 offset:0
	global_load_dwordx4 v[156:159], v197, s[6:7]
	v_mfma_f32_16x16x32_bf16 v[48:51], v[180:183], v[242:245], v[48:51]
	v_add_f32_e32 v221, v221, v85
	v_add_f32_e32 v220, v220, v82
	v_mfma_f32_16x16x32_bf16 v[52:55], v[180:183], v[204:207], v[52:55]
	v_add_f32_e32 v221, v221, v86
	ds_read_b128 v[180:183], v209 offset:53248
	s_waitcnt lgkmcnt(6)
	v_mfma_f32_16x16x32_bf16 v[92:95], v[230:233], v[124:127], v[92:95]
	v_add_f32_e32 v220, v220, v83
	v_add_f32_e32 v221, v221, v87
	v_mfma_f32_16x16x32_bf16 v[88:91], v[230:233], v[108:111], v[88:91]
	v_cvt_pk_bf16_f32 v218, v72, v73
	ds_read_b128 v[230:233], v246 offset:0
	v_mfma_f32_16x16x32_bf16 v[60:63], v[234:237], v[204:207], v[60:63]
	v_cvt_pk_bf16_f32 v219, v74, v75
	v_cvt_pk_bf16_f32 v240, v76, v77
	v_mfma_f32_16x16x32_bf16 v[56:59], v[234:237], v[242:245], v[56:59]
	v_cvt_pk_bf16_f32 v241, v78, v79
	ds_read_b128 v[234:237], v209 offset:55296
	s_setprio 0
	s_waitcnt lgkmcnt(6)
	v_mfma_f32_16x16x32_bf16 v[64:67], v[160:163], v[96:99], 0
	v_exp_f32_e32 v88, v88
	v_mfma_f32_16x16x32_bf16 v[68:71], v[160:163], v[112:115], 0
	v_exp_f32_e32 v92, v92
	ds_read_b128 v[160:163], v201 offset:4096
	s_add_u32 s6, s15, 0x23a80000
	s_addc_u32 s7, s14, 0
	v_mfma_f32_16x16x32_bf16 v[0:3], v[164:167], v[216:219], v[0:3]
	v_cvt_pk_bf16_f32 v242, v80, v81
	v_mfma_f32_16x16x32_bf16 v[4:7], v[164:167], v[238:241], v[4:7]
	v_exp_f32_e32 v89, v89
	ds_read_b128 v[164:167], v209 offset:57344
	s_waitcnt vmcnt(4)
	ds_write_b128 v225, v[136:139] offset:32768
	s_waitcnt lgkmcnt(7)
	v_mfma_f32_16x16x32_bf16 v[68:71], v[168:171], v[116:119], v[68:71]
	v_exp_f32_e32 v93, v93
	v_mfma_f32_16x16x32_bf16 v[64:67], v[168:171], v[100:103], v[64:67]
	v_cvt_pk_bf16_f32 v243, v82, v83
	ds_read_b128 v[168:171], v202 offset:4096
	v_mfma_f32_16x16x32_bf16 v[12:15], v[172:175], v[238:241], v[12:15]
	v_exp_f32_e32 v90, v90
	v_mfma_f32_16x16x32_bf16 v[8:11], v[172:175], v[216:219], v[8:11]
	v_exp_f32_e32 v94, v94
	ds_read_b128 v[172:175], v209 offset:59392
	s_waitcnt lgkmcnt(7)
	v_mfma_f32_16x16x32_bf16 v[64:67], v[176:179], v[104:107], v[64:67]
	v_cvt_pk_bf16_f32 v204, v84, v85
	v_mfma_f32_16x16x32_bf16 v[68:71], v[176:179], v[120:123], v[68:71]
	v_exp_f32_e32 v91, v91
	ds_read_b128 v[176:179], v203 offset:4096
	ds_write_b128 v226, v[140:143] offset:32768
	v_mfma_f32_16x16x32_bf16 v[16:19], v[180:183], v[216:219], v[16:19]
	v_exp_f32_e32 v95, v95
	v_mfma_f32_16x16x32_bf16 v[20:23], v[180:183], v[238:241], v[20:23]
	v_cvt_pk_bf16_f32 v205, v86, v87
	v_add_f32_e32 v220, v220, v88
	ds_read_b128 v[180:183], v209 offset:61440
	s_waitcnt lgkmcnt(8)
	v_mfma_f32_16x16x32_bf16 v[68:71], v[230:233], v[124:127], v[68:71]
	v_add_f32_e32 v221, v221, v92
	v_add_f32_e32 v220, v220, v89
	v_mfma_f32_16x16x32_bf16 v[64:67], v[230:233], v[108:111], v[64:67]
	v_add_f32_e32 v221, v221, v93
	v_cvt_pk_bf16_f32 v244, v88, v89
	ds_read_b128 v[230:233], v246 offset:4096
	v_mfma_f32_16x16x32_bf16 v[28:31], v[234:237], v[238:241], v[28:31]
	v_cvt_pk_bf16_f32 v245, v90, v91
	v_cvt_pk_bf16_f32 v206, v92, v93
	v_mfma_f32_16x16x32_bf16 v[24:27], v[234:237], v[216:219], v[24:27]
	v_cvt_pk_bf16_f32 v207, v94, v95
	ds_read_b128 v[234:237], v209 offset:63488
	ds_write_b64 v227, v[148:149] offset:16384
	s_waitcnt lgkmcnt(9)
	v_mfma_f32_16x16x32_bf16 v[72:75], v[160:163], v[96:99], 0
	v_add_f32_e32 v220, v220, v90
	v_add_f32_e32 v221, v221, v94
	v_mfma_f32_16x16x32_bf16 v[76:79], v[160:163], v[112:115], 0
	v_add_f32_e32 v220, v220, v91
	v_add_f32_e32 v221, v221, v95
	ds_read_b128 v[160:163], v201 offset:8192
	v_mfma_f32_16x16x32_bf16 v[32:35], v[164:167], v[216:219], v[32:35]
	v_add_f32_e32 v194, v194, v220
	v_add_f32_e32 v195, v195, v221
	v_mfma_f32_16x16x32_bf16 v[36:39], v[164:167], v[238:241], v[36:39]
	v_exp_f32_e32 v64, v64
	ds_read_b128 v[164:167], v210 offset:49152
	s_waitcnt lgkmcnt(8)
	v_mfma_f32_16x16x32_bf16 v[76:79], v[168:171], v[116:119], v[76:79]
	v_exp_f32_e32 v68, v68
	v_mfma_f32_16x16x32_bf16 v[72:75], v[168:171], v[100:103], v[72:75]
	v_exp_f32_e32 v65, v65
	ds_read_b128 v[168:171], v202 offset:8192
	ds_write_b64 v228, v[150:151] offset:16384
	v_mfma_f32_16x16x32_bf16 v[44:47], v[172:175], v[238:241], v[44:47]
	v_exp_f32_e32 v69, v69
	v_mfma_f32_16x16x32_bf16 v[40:43], v[172:175], v[216:219], v[40:43]
	v_exp_f32_e32 v66, v66
	ds_read_b128 v[172:175], v210 offset:51200
	s_waitcnt lgkmcnt(8)
	v_mfma_f32_16x16x32_bf16 v[72:75], v[176:179], v[104:107], v[72:75]
	v_exp_f32_e32 v70, v70
	v_mfma_f32_16x16x32_bf16 v[76:79], v[176:179], v[120:123], v[76:79]
	v_exp_f32_e32 v67, v67
	ds_read_b128 v[176:179], v203 offset:8192
	v_mfma_f32_16x16x32_bf16 v[48:51], v[180:183], v[216:219], v[48:51]
	v_exp_f32_e32 v71, v71
	v_mfma_f32_16x16x32_bf16 v[52:55], v[180:183], v[238:241], v[52:55]
	v_add_f32_e32 v220, v64, v65
	ds_read_b128 v[180:183], v210 offset:53248
	ds_write_b64 v229, v[144:145] offset:16384
	s_waitcnt lgkmcnt(9)
	v_mfma_f32_16x16x32_bf16 v[76:79], v[230:233], v[124:127], v[76:79]
	v_add_f32_e32 v221, v68, v69
	v_mfma_f32_16x16x32_bf16 v[72:75], v[230:233], v[108:111], v[72:75]
	v_add_f32_e32 v220, v220, v66
	ds_read_b128 v[230:233], v246 offset:8192
	v_mfma_f32_16x16x32_bf16 v[60:63], v[234:237], v[238:241], v[60:63]
	v_add_f32_e32 v221, v221, v70
	v_add_f32_e32 v220, v220, v67
	v_mfma_f32_16x16x32_bf16 v[56:59], v[234:237], v[216:219], v[56:59]
	v_add_f32_e32 v221, v221, v71
	ds_read_b128 v[234:237], v210 offset:55296
	s_waitcnt lgkmcnt(8)
	v_mfma_f32_16x16x32_bf16 v[80:83], v[160:163], v[96:99], 0
	v_exp_f32_e32 v72, v72
	v_mfma_f32_16x16x32_bf16 v[84:87], v[160:163], v[112:115], 0
	v_exp_f32_e32 v76, v76
	ds_read_b128 v[160:163], v201 offset:12288
	ds_write_b64 v184, v[146:147] offset:16384
	v_mfma_f32_16x16x32_bf16 v[0:3], v[164:167], v[242:245], v[0:3]
	v_exp_f32_e32 v73, v73
	v_mfma_f32_16x16x32_bf16 v[4:7], v[164:167], v[204:207], v[4:7]
	v_exp_f32_e32 v77, v77
	ds_read_b128 v[164:167], v210 offset:57344
	s_waitcnt lgkmcnt(8)
	v_mfma_f32_16x16x32_bf16 v[84:87], v[168:171], v[116:119], v[84:87]
	v_exp_f32_e32 v74, v74
	v_mfma_f32_16x16x32_bf16 v[80:83], v[168:171], v[100:103], v[80:83]
	v_exp_f32_e32 v78, v78
	ds_read_b128 v[168:171], v202 offset:12288
	v_mfma_f32_16x16x32_bf16 v[12:15], v[172:175], v[204:207], v[12:15]
	v_exp_f32_e32 v75, v75
	v_mfma_f32_16x16x32_bf16 v[8:11], v[172:175], v[242:245], v[8:11]
	v_exp_f32_e32 v79, v79
	ds_read_b128 v[172:175], v210 offset:59392
	global_load_dwordx4 v[148:151], v198, s[8:9] offset:384
	s_waitcnt lgkmcnt(8)
	v_mfma_f32_16x16x32_bf16 v[80:83], v[176:179], v[104:107], v[80:83]
	v_add_f32_e32 v220, v220, v72
	v_add_f32_e32 v221, v221, v76
	v_mfma_f32_16x16x32_bf16 v[84:87], v[176:179], v[120:123], v[84:87]
	v_add_f32_e32 v220, v220, v73
	ds_read_b128 v[176:179], v203 offset:12288
	v_mfma_f32_16x16x32_bf16 v[16:19], v[180:183], v[242:245], v[16:19]
	v_add_f32_e32 v221, v221, v77
	v_add_f32_e32 v220, v220, v74
	v_mfma_f32_16x16x32_bf16 v[20:23], v[180:183], v[204:207], v[20:23]
	v_add_f32_e32 v221, v221, v78
	ds_read_b128 v[180:183], v210 offset:61440
	s_waitcnt lgkmcnt(7)
	v_mfma_f32_16x16x32_bf16 v[84:87], v[230:233], v[124:127], v[84:87]
	v_add_f32_e32 v220, v220, v75
	v_add_f32_e32 v221, v221, v79
	v_mfma_f32_16x16x32_bf16 v[80:83], v[230:233], v[108:111], v[80:83]
	v_cvt_pk_bf16_f32 v216, v64, v65
	ds_read_b128 v[230:233], v246 offset:12288
	global_load_dwordx4 v[144:147], v199, s[8:9] offset:384
	v_mfma_f32_16x16x32_bf16 v[28:31], v[234:237], v[204:207], v[28:31]
	v_cvt_pk_bf16_f32 v217, v66, v67
	v_cvt_pk_bf16_f32 v238, v68, v69
	v_mfma_f32_16x16x32_bf16 v[24:27], v[234:237], v[242:245], v[24:27]
	v_cvt_pk_bf16_f32 v239, v70, v71
	ds_read_b128 v[234:237], v210 offset:63488
	s_waitcnt lgkmcnt(6)
	v_mfma_f32_16x16x32_bf16 v[88:91], v[160:163], v[96:99], 0
	v_exp_f32_e32 v80, v80
	v_mfma_f32_16x16x32_bf16 v[92:95], v[160:163], v[112:115], 0
	v_exp_f32_e32 v84, v84
	v_mfma_f32_16x16x32_bf16 v[32:35], v[164:167], v[242:245], v[32:35]
	v_exp_f32_e32 v81, v81
	v_mfma_f32_16x16x32_bf16 v[36:39], v[164:167], v[204:207], v[36:39]
	v_exp_f32_e32 v85, v85
	global_load_dwordx4 v[136:139], v196, s[6:7]
	s_waitcnt lgkmcnt(4)
	v_mfma_f32_16x16x32_bf16 v[92:95], v[168:171], v[116:119], v[92:95]
	v_exp_f32_e32 v82, v82
	v_mfma_f32_16x16x32_bf16 v[88:91], v[168:171], v[100:103], v[88:91]
	v_exp_f32_e32 v86, v86
	v_mfma_f32_16x16x32_bf16 v[44:47], v[172:175], v[204:207], v[44:47]
	v_exp_f32_e32 v83, v83
	v_mfma_f32_16x16x32_bf16 v[40:43], v[172:175], v[242:245], v[40:43]
	v_exp_f32_e32 v87, v87
	s_waitcnt lgkmcnt(3)
	v_mfma_f32_16x16x32_bf16 v[88:91], v[176:179], v[104:107], v[88:91]
	v_add_f32_e32 v220, v220, v80
	v_add_f32_e32 v221, v221, v84
	v_mfma_f32_16x16x32_bf16 v[92:95], v[176:179], v[120:123], v[92:95]
	v_add_f32_e32 v220, v220, v81
	global_load_dwordx4 v[140:143], v197, s[6:7]
	s_waitcnt lgkmcnt(0)
	s_barrier
	ds_read_b128 v[160:163], v201 offset:16384
	ds_read_b128 v[164:167], v209 offset:0
	ds_read_b128 v[168:171], v202 offset:16384
	ds_read_b128 v[172:175], v209 offset:2048
	ds_read_b128 v[176:179], v203 offset:16384
	v_mfma_f32_16x16x32_bf16 v[48:51], v[180:183], v[242:245], v[48:51]
	v_add_f32_e32 v221, v221, v85
	v_add_f32_e32 v220, v220, v82
	v_mfma_f32_16x16x32_bf16 v[52:55], v[180:183], v[204:207], v[52:55]
	v_add_f32_e32 v221, v221, v86
	ds_read_b128 v[180:183], v209 offset:4096
	v_mfma_f32_16x16x32_bf16 v[92:95], v[230:233], v[124:127], v[92:95]
	v_add_f32_e32 v220, v220, v83
	v_add_f32_e32 v221, v221, v87
	v_mfma_f32_16x16x32_bf16 v[88:91], v[230:233], v[108:111], v[88:91]
	v_cvt_pk_bf16_f32 v218, v72, v73
	ds_read_b128 v[230:233], v246 offset:16384
	s_add_u32 s8, s8, 0x200
	s_addc_u32 s9, s9, 0
	s_add_u32 s12, s12, 0x40000
	s_addc_u32 s13, s13, 0
	s_add_i32 s4, s4, 4
	s_cmp_lt_u32 s4, s101
	s_cselect_b64 vcc, -1, 0
	v_mfma_f32_16x16x32_bf16 v[60:63], v[234:237], v[204:207], v[60:63]
	v_cvt_pk_bf16_f32 v219, v74, v75
	v_cvt_pk_bf16_f32 v240, v76, v77
	v_mfma_f32_16x16x32_bf16 v[56:59], v[234:237], v[242:245], v[56:59]
	v_cvt_pk_bf16_f32 v241, v78, v79
	ds_read_b128 v[234:237], v209 offset:6144
	s_cbranch_vccnz .LBB0_734
	s_setprio 0
	s_waitcnt vmcnt(0)
	s_nop 7
	s_nop 7
	ds_swizzle_b32 v64, v194 offset:swizzle(SWAP,16)
	s_waitcnt lgkmcnt(0)
	v_add_f32_e32 v194, v194, v64
	v_mov_b32_e32 v65, v194
	s_nop 1
	v_permlane32_swap_b32_e32 v194, v65
	v_add_f32_e32 v194, v194, v65
	s_nop 0
	v_rcp_f32_e32 v66, v194
	ds_swizzle_b32 v64, v195 offset:swizzle(SWAP,16)
	s_waitcnt lgkmcnt(0)
	v_add_f32_e32 v195, v195, v64
	v_mov_b32_e32 v65, v195
	s_nop 1
	v_permlane32_swap_b32_e32 v195, v65
	v_add_f32_e32 v195, v195, v65
	s_nop 0
	v_rcp_f32_e32 v67, v195
	v_readlane_b32 s100, v250, 8
	v_mbcnt_lo_u32_b32 v68, -1, 0
	v_mbcnt_hi_u32_b32 v68, -1, v68
	v_and_b32_e32 v69, 15, v68
	v_lshrrev_b32_e32 v70, 4, v68
	s_lshr_b32 s101, s100, 1
	v_add_u32_e32 v69, s101, v69
	v_lshlrev_b32_e32 v69, 12, v69
	v_and_b32_e32 v71, 1, v70
	v_lshlrev_b32_e32 v71, 5, v71
	v_and_b32_e32 v70, 2, v70
	v_lshl_add_u32 v71, v70, 3, v71
	v_add_u32_e32 v70, v69, v71
	v_add_u32_e32 v71, 0x10000, v70
	v_mul_f32_e32 v0, v0, v66
	v_mul_f32_e32 v1, v1, v66
	v_mul_f32_e32 v2, v2, v66
	v_mul_f32_e32 v3, v3, v66
	v_mul_f32_e32 v8, v8, v66
	v_mul_f32_e32 v9, v9, v66
	v_mul_f32_e32 v10, v10, v66
	v_mul_f32_e32 v11, v11, v66
	v_cvt_pk_bf16_f32 v72, v0, v1
	v_cvt_pk_bf16_f32 v73, v2, v3
	v_cvt_pk_bf16_f32 v74, v8, v9
	v_cvt_pk_bf16_f32 v75, v10, v11
	s_nop 1
	v_permlane16_swap_b32_e32 v72, v74
	v_permlane16_swap_b32_e32 v73, v75
	s_nop 1
	global_store_dwordx4 v70, v[72:75], s[58:59] offset:0
	v_mul_f32_e32 v16, v16, v66
	v_mul_f32_e32 v17, v17, v66
	v_mul_f32_e32 v18, v18, v66
	v_mul_f32_e32 v19, v19, v66
	v_mul_f32_e32 v24, v24, v66
	v_mul_f32_e32 v25, v25, v66
	v_mul_f32_e32 v26, v26, v66
	v_mul_f32_e32 v27, v27, v66
	v_cvt_pk_bf16_f32 v76, v16, v17
	v_cvt_pk_bf16_f32 v77, v18, v19
	v_cvt_pk_bf16_f32 v78, v24, v25
	v_cvt_pk_bf16_f32 v79, v26, v27
	s_nop 1
	v_permlane16_swap_b32_e32 v76, v78
	v_permlane16_swap_b32_e32 v77, v79
	s_nop 1
	global_store_dwordx4 v70, v[76:79], s[58:59] offset:64
	v_mul_f32_e32 v32, v32, v66
	v_mul_f32_e32 v33, v33, v66
	v_mul_f32_e32 v34, v34, v66
	v_mul_f32_e32 v35, v35, v66
	v_mul_f32_e32 v40, v40, v66
	v_mul_f32_e32 v41, v41, v66
	v_mul_f32_e32 v42, v42, v66
	v_mul_f32_e32 v43, v43, v66
	v_cvt_pk_bf16_f32 v80, v32, v33
	v_cvt_pk_bf16_f32 v81, v34, v35
	v_cvt_pk_bf16_f32 v82, v40, v41
	v_cvt_pk_bf16_f32 v83, v42, v43
	s_nop 1
	v_permlane16_swap_b32_e32 v80, v82
	v_permlane16_swap_b32_e32 v81, v83
	s_nop 1
	global_store_dwordx4 v70, v[80:83], s[58:59] offset:128
	v_mul_f32_e32 v48, v48, v66
	v_mul_f32_e32 v49, v49, v66
	v_mul_f32_e32 v50, v50, v66
	v_mul_f32_e32 v51, v51, v66
	v_mul_f32_e32 v56, v56, v66
	v_mul_f32_e32 v57, v57, v66
	v_mul_f32_e32 v58, v58, v66
	v_mul_f32_e32 v59, v59, v66
	v_cvt_pk_bf16_f32 v84, v48, v49
	v_cvt_pk_bf16_f32 v85, v50, v51
	v_cvt_pk_bf16_f32 v86, v56, v57
	v_cvt_pk_bf16_f32 v87, v58, v59
	s_nop 1
	v_permlane16_swap_b32_e32 v84, v86
	v_permlane16_swap_b32_e32 v85, v87
	s_nop 1
	global_store_dwordx4 v70, v[84:87], s[58:59] offset:192
	v_mul_f32_e32 v4, v4, v67
	v_mul_f32_e32 v5, v5, v67
	v_mul_f32_e32 v6, v6, v67
	v_mul_f32_e32 v7, v7, v67
	v_mul_f32_e32 v12, v12, v67
	v_mul_f32_e32 v13, v13, v67
	v_mul_f32_e32 v14, v14, v67
	v_mul_f32_e32 v15, v15, v67
	v_cvt_pk_bf16_f32 v88, v4, v5
	v_cvt_pk_bf16_f32 v89, v6, v7
	v_cvt_pk_bf16_f32 v90, v12, v13
	v_cvt_pk_bf16_f32 v91, v14, v15
	s_nop 1
	v_permlane16_swap_b32_e32 v88, v90
	v_permlane16_swap_b32_e32 v89, v91
	s_nop 1
	global_store_dwordx4 v71, v[88:91], s[58:59] offset:0
	v_mul_f32_e32 v20, v20, v67
	v_mul_f32_e32 v21, v21, v67
	v_mul_f32_e32 v22, v22, v67
	v_mul_f32_e32 v23, v23, v67
	v_mul_f32_e32 v28, v28, v67
	v_mul_f32_e32 v29, v29, v67
	v_mul_f32_e32 v30, v30, v67
	v_mul_f32_e32 v31, v31, v67
	v_cvt_pk_bf16_f32 v92, v20, v21
	v_cvt_pk_bf16_f32 v93, v22, v23
	v_cvt_pk_bf16_f32 v94, v28, v29
	v_cvt_pk_bf16_f32 v95, v30, v31
	s_nop 1
	v_permlane16_swap_b32_e32 v92, v94
	v_permlane16_swap_b32_e32 v93, v95
	s_nop 1
	global_store_dwordx4 v71, v[92:95], s[58:59] offset:64
	v_mul_f32_e32 v36, v36, v67
	v_mul_f32_e32 v37, v37, v67
	v_mul_f32_e32 v38, v38, v67
	v_mul_f32_e32 v39, v39, v67
	v_mul_f32_e32 v44, v44, v67
	v_mul_f32_e32 v45, v45, v67
	v_mul_f32_e32 v46, v46, v67
	v_mul_f32_e32 v47, v47, v67
	v_cvt_pk_bf16_f32 v72, v36, v37
	v_cvt_pk_bf16_f32 v73, v38, v39
	v_cvt_pk_bf16_f32 v74, v44, v45
	v_cvt_pk_bf16_f32 v75, v46, v47
	s_nop 1
	v_permlane16_swap_b32_e32 v72, v74
	v_permlane16_swap_b32_e32 v73, v75
	s_nop 1
	global_store_dwordx4 v71, v[72:75], s[58:59] offset:128
	v_mul_f32_e32 v52, v52, v67
	v_mul_f32_e32 v53, v53, v67
	v_mul_f32_e32 v54, v54, v67
	v_mul_f32_e32 v55, v55, v67
	v_mul_f32_e32 v60, v60, v67
	v_mul_f32_e32 v61, v61, v67
	v_mul_f32_e32 v62, v62, v67
	v_mul_f32_e32 v63, v63, v67
	v_cvt_pk_bf16_f32 v76, v52, v53
	v_cvt_pk_bf16_f32 v77, v54, v55
	v_cvt_pk_bf16_f32 v78, v60, v61
	v_cvt_pk_bf16_f32 v79, v62, v63
	s_nop 1
	v_permlane16_swap_b32_e32 v76, v78
	v_permlane16_swap_b32_e32 v77, v79
	s_nop 1
	global_store_dwordx4 v71, v[76:79], s[58:59] offset:192
	s_barrier
